# four-waves-per-row version with the 1 KB pieces of a row interleaved among the four waves (wave h reads pieces h, h+4, ...) instead of contiguous quarters
# baseline (speedup 1.0000x reference)
_Z11attn_kernelPKfS0_PKDv8_DF16_S0_Pfi:
	s_load_dwordx2 s[28:29], s[0:1], 0x0
	v_cmp_gt_u32_e32 vcc, 16, v0
	s_and_saveexec_b64 s[4:5], vcc
	v_lshlrev_b32_e32 v1, 2, v0
	v_mov_b32_e32 v2, 0
	ds_write_b32 v1, v2 offset:36864
	s_or_b64 exec, exec, s[4:5]
	s_load_dword s33, s[0:1], 0x28
	v_bfe_u32 v1, v0, 6, 2
	v_lshl_or_b32 v82, s2, 2, v1
	v_readfirstlane_b32 s34, v0
	s_cmp_gt_u32 s34, 0xff
	s_cbranch_scc1 .Lsc_early_skip
	v_and_b32_e32 v3, 63, v0
	v_lshlrev_b32_e32 v2, 4, v3
	s_lshr_b32 s55, s34, 6
	s_mul_i32 s43, s55, 0x400
	s_and_b32 s56, s2, 7
	s_lshr_b32 s57, s2, 3
	s_mul_i32 s37, s56, 31
	s_min_u32 s56, s56, 2
	s_add_u32 s37, s37, s56
	s_add_u32 s37, s37, s57
	s_and_b32 s47, s37, 1
	s_lshl_b32 s47, s47, 2
	s_mul_i32 s38, s37, 0x9c40
	s_lshl_b32 s40, s47, 4
	s_sub_u32 s38, s38, s40
	s_add_u32 s38, s38, s43
	s_waitcnt lgkmcnt(0)
	s_and_b32 s29, s29, 0xffff
	s_mov_b32 s30, 0x17d78400
	s_mov_b32 s31, 0x20000
	v_mov_b32_e32 v12, v2
	v_mov_b32_e32 v4, v2
	s_cmp_lg_u32 s55, 0
	s_cbranch_scc1 .Lsc_flpa
	v_max_u32_e32 v12, s47, v3
	v_lshlrev_b32_e32 v12, 4, v12

.Lsc_flpb:
	buffer_load_dwordx4 v[100:103], v12, s[28:31], s38 offen nt
	s_add_u32 s40, s38, 0x1000
	buffer_load_dwordx4 v[104:107], v2, s[28:31], s40 offen nt
	s_add_u32 s40, s38, 0x2000
	buffer_load_dwordx4 v[108:111], v2, s[28:31], s40 offen nt
	s_add_u32 s40, s38, 0x3000
	buffer_load_dwordx4 v[112:115], v2, s[28:31], s40 offen nt
	s_add_u32 s40, s38, 0x4000
	buffer_load_dwordx4 v[116:119], v2, s[28:31], s40 offen nt
	s_add_u32 s40, s38, 0x5000
	buffer_load_dwordx4 v[120:123], v2, s[28:31], s40 offen nt
	s_add_u32 s40, s38, 0x6000
	buffer_load_dwordx4 v[124:127], v2, s[28:31], s40 offen nt
	s_add_u32 s40, s38, 0x7000
	buffer_load_dwordx4 v[128:131], v2, s[28:31], s40 offen nt
	s_add_u32 s40, s38, 0x8000
	buffer_load_dwordx4 v[132:135], v2, s[28:31], s40 offen nt
	s_add_u32 s40, s38, 0x9000
	buffer_load_dwordx4 v[136:139], v4, s[28:31], s40 offen nt

.LBB1_217:
	s_andn2_saveexec_b64 s[0:1], s[30:31]
	s_cbranch_execz .LBB1_384
	v_readfirstlane_b32 s34, v1
	v_readfirstlane_b32 s36, v84
	v_and_b32_e32 v3, 63, v0
	v_lshlrev_b32_e32 v2, 4, v3
	s_cmp_lt_i32 s36, 0
	s_cbranch_scc1 .LBB1_384
	s_add_i32 s36, s36, 1
	s_lshl_b32 s36, s36, 2
	s_sub_i32 s36, s36, 1
	s_lshr_b32 s33, s33, 2
	s_mov_b32 s55, s34
	s_mul_i32 s43, s55, 0x400
	s_and_b32 s56, s2, 7
	s_lshr_b32 s57, s2, 3
	s_mul_i32 s37, s56, 31
	s_min_u32 s56, s56, 2
	s_add_u32 s37, s37, s56
	s_add_u32 s37, s37, s57
	s_waitcnt lgkmcnt(0)
	s_and_b32 s29, s29, 0xffff
	s_mov_b32 s30, 0x17d78400
	s_mov_b32 s31, 0x20000
	s_mov_b32 s35, 0
	s_movk_i32 s7, 0x40
	s_mov_b32 s9, 0x7fffffff
	s_lshl_b32 s44, s34, 12
	s_add_u32 s44, s44, 0x4000
	s_lshl_b32 s45, s34, 10
	s_add_u32 s45, s45, 0x8000
	s_lshl_b32 s46, s34, 4
	s_add_u32 s46, s46, 0x9000
	s_and_b32 s47, s37, 1
	s_lshl_b32 s47, s47, 2
	s_mul_i32 s38, s37, 0x9c40
	s_lshl_b32 s40, s47, 4
	s_sub_u32 s38, s38, s40
	s_add_u32 s38, s38, s43
.Lsc_row:
	v_subrev_u32_e32 v8, s47, v3
	v_lshlrev_b32_e32 v8, 2, v8
	s_mul_i32 s40, s55, 0x100
	v_add_u32_e32 v8, s40, v8
	s_mov_b64 s[48:49], -1
	s_mov_b64 s[50:51], -1
	s_cmp_lg_u32 s55, 0
	s_cbranch_scc1 .Lsc_m0
	s_lshl_b64 s[48:49], -1, s47

.Lsc_s0:
	s_mov_b32 s40, s39
	buffer_load_dwordx4 v[100:103], v5, s[28:31], s40 offen nt
	s_waitcnt vmcnt(9)
	v_or3_b32 v12, v104, v105, v106
	v_bitop3_b32 v12, v12, s9, v107 bitop3:0xc8
	v_cmp_ne_u32_e32 vcc, 0, v12
	s_cbranch_vccz .Lsc_s1
	s_bcnt1_i32_b64 s40, vcc
	v_mbcnt_lo_u32_b32 v13, vcc_lo, 0
	v_mbcnt_hi_u32_b32 v13, vcc_hi, v13
	v_add_u32_e32 v13, s42, v13
	s_add_i32 s42, s42, s40
	v_cmp_gt_i32_e64 s[0:1], s7, v13
	s_and_b64 s[4:5], vcc, s[0:1]
	s_and_saveexec_b64 s[0:1], s[4:5]
	v_lshl_add_u32 v14, v13, 4, v9
	v_lshl_add_u32 v15, v13, 2, v10
	v_add_u32_e32 v13, 0x400, v8
	ds_write_b128 v14, v[104:107]
	ds_write_b32 v15, v13
	s_mov_b64 exec, -1
.Lsc_s1:
	s_add_u32 s40, s39, 0x1000
	buffer_load_dwordx4 v[104:107], v6, s[28:31], s40 offen nt
	s_waitcnt vmcnt(9)
	v_or3_b32 v12, v108, v109, v110
	v_bitop3_b32 v12, v12, s9, v111 bitop3:0xc8
	v_cmp_ne_u32_e32 vcc, 0, v12
	s_cbranch_vccz .Lsc_s2
	s_bcnt1_i32_b64 s40, vcc
	v_mbcnt_lo_u32_b32 v13, vcc_lo, 0
	v_mbcnt_hi_u32_b32 v13, vcc_hi, v13
	v_add_u32_e32 v13, s42, v13
	s_add_i32 s42, s42, s40
	v_cmp_gt_i32_e64 s[0:1], s7, v13
	s_and_b64 s[4:5], vcc, s[0:1]
	s_and_saveexec_b64 s[0:1], s[4:5]
	v_lshl_add_u32 v14, v13, 4, v9
	v_lshl_add_u32 v15, v13, 2, v10
	v_add_u32_e32 v13, 0x800, v8
	ds_write_b128 v14, v[108:111]
	ds_write_b32 v15, v13
	s_mov_b64 exec, -1
.Lsc_s2:
	s_add_u32 s40, s39, 0x2000
	buffer_load_dwordx4 v[108:111], v6, s[28:31], s40 offen nt
	s_waitcnt vmcnt(9)
	v_or3_b32 v12, v112, v113, v114
	v_bitop3_b32 v12, v12, s9, v115 bitop3:0xc8
	v_cmp_ne_u32_e32 vcc, 0, v12
	s_cbranch_vccz .Lsc_s3
	s_bcnt1_i32_b64 s40, vcc
	v_mbcnt_lo_u32_b32 v13, vcc_lo, 0
	v_mbcnt_hi_u32_b32 v13, vcc_hi, v13
	v_add_u32_e32 v13, s42, v13
	s_add_i32 s42, s42, s40
	v_cmp_gt_i32_e64 s[0:1], s7, v13
	s_and_b64 s[4:5], vcc, s[0:1]
	s_and_saveexec_b64 s[0:1], s[4:5]
	v_lshl_add_u32 v14, v13, 4, v9
	v_lshl_add_u32 v15, v13, 2, v10
	v_add_u32_e32 v13, 0xc00, v8
	ds_write_b128 v14, v[112:115]
	ds_write_b32 v15, v13
	s_mov_b64 exec, -1
.Lsc_s3:
	s_add_u32 s40, s39, 0x3000
	buffer_load_dwordx4 v[112:115], v6, s[28:31], s40 offen nt
	s_waitcnt vmcnt(9)
	v_or3_b32 v12, v116, v117, v118
	v_bitop3_b32 v12, v12, s9, v119 bitop3:0xc8
	v_cmp_ne_u32_e32 vcc, 0, v12
	s_cbranch_vccz .Lsc_s4
	s_bcnt1_i32_b64 s40, vcc
	v_mbcnt_lo_u32_b32 v13, vcc_lo, 0
	v_mbcnt_hi_u32_b32 v13, vcc_hi, v13
	v_add_u32_e32 v13, s42, v13
	s_add_i32 s42, s42, s40
	v_cmp_gt_i32_e64 s[0:1], s7, v13
	s_and_b64 s[4:5], vcc, s[0:1]
	s_and_saveexec_b64 s[0:1], s[4:5]
	v_lshl_add_u32 v14, v13, 4, v9
	v_lshl_add_u32 v15, v13, 2, v10
	v_add_u32_e32 v13, 0x1000, v8
	ds_write_b128 v14, v[116:119]
	ds_write_b32 v15, v13
	s_mov_b64 exec, -1
.Lsc_s4:
	s_add_u32 s40, s39, 0x4000
	buffer_load_dwordx4 v[116:119], v6, s[28:31], s40 offen nt
	s_waitcnt vmcnt(9)
	v_or3_b32 v12, v120, v121, v122
	v_bitop3_b32 v12, v12, s9, v123 bitop3:0xc8
	v_cmp_ne_u32_e32 vcc, 0, v12
	s_cbranch_vccz .Lsc_s5
	s_bcnt1_i32_b64 s40, vcc
	v_mbcnt_lo_u32_b32 v13, vcc_lo, 0
	v_mbcnt_hi_u32_b32 v13, vcc_hi, v13
	v_add_u32_e32 v13, s42, v13
	s_add_i32 s42, s42, s40
	v_cmp_gt_i32_e64 s[0:1], s7, v13
	s_and_b64 s[4:5], vcc, s[0:1]
	s_and_saveexec_b64 s[0:1], s[4:5]
	v_lshl_add_u32 v14, v13, 4, v9
	v_lshl_add_u32 v15, v13, 2, v10
	v_add_u32_e32 v13, 0x1400, v8
	ds_write_b128 v14, v[120:123]
	ds_write_b32 v15, v13
	s_mov_b64 exec, -1
.Lsc_s5:
	s_add_u32 s40, s39, 0x5000
	buffer_load_dwordx4 v[120:123], v6, s[28:31], s40 offen nt
	s_waitcnt vmcnt(9)
	v_or3_b32 v12, v124, v125, v126
	v_bitop3_b32 v12, v12, s9, v127 bitop3:0xc8
	v_cmp_ne_u32_e32 vcc, 0, v12
	s_cbranch_vccz .Lsc_s6
	s_bcnt1_i32_b64 s40, vcc
	v_mbcnt_lo_u32_b32 v13, vcc_lo, 0
	v_mbcnt_hi_u32_b32 v13, vcc_hi, v13
	v_add_u32_e32 v13, s42, v13
	s_add_i32 s42, s42, s40
	v_cmp_gt_i32_e64 s[0:1], s7, v13
	s_and_b64 s[4:5], vcc, s[0:1]
	s_and_saveexec_b64 s[0:1], s[4:5]
	v_lshl_add_u32 v14, v13, 4, v9
	v_lshl_add_u32 v15, v13, 2, v10
	v_add_u32_e32 v13, 0x1800, v8
	ds_write_b128 v14, v[124:127]
	ds_write_b32 v15, v13
	s_mov_b64 exec, -1
.Lsc_s6:
	s_add_u32 s40, s39, 0x6000
	buffer_load_dwordx4 v[124:127], v6, s[28:31], s40 offen nt
	s_waitcnt vmcnt(9)
	v_or3_b32 v12, v128, v129, v130
	v_bitop3_b32 v12, v12, s9, v131 bitop3:0xc8
	v_cmp_ne_u32_e32 vcc, 0, v12
	s_cbranch_vccz .Lsc_s7
	s_bcnt1_i32_b64 s40, vcc
	v_mbcnt_lo_u32_b32 v13, vcc_lo, 0
	v_mbcnt_hi_u32_b32 v13, vcc_hi, v13
	v_add_u32_e32 v13, s42, v13
	s_add_i32 s42, s42, s40
	v_cmp_gt_i32_e64 s[0:1], s7, v13
	s_and_b64 s[4:5], vcc, s[0:1]
	s_and_saveexec_b64 s[0:1], s[4:5]
	v_lshl_add_u32 v14, v13, 4, v9
	v_lshl_add_u32 v15, v13, 2, v10
	v_add_u32_e32 v13, 0x1c00, v8
	ds_write_b128 v14, v[128:131]
	ds_write_b32 v15, v13
	s_mov_b64 exec, -1
.Lsc_s7:
	s_add_u32 s40, s39, 0x7000
	buffer_load_dwordx4 v[128:131], v6, s[28:31], s40 offen nt
	s_waitcnt vmcnt(9)
	v_or3_b32 v12, v132, v133, v134
	v_bitop3_b32 v12, v12, s9, v135 bitop3:0xc8
	v_cmp_ne_u32_e32 vcc, 0, v12
	s_cbranch_vccz .Lsc_s8
	s_bcnt1_i32_b64 s40, vcc
	v_mbcnt_lo_u32_b32 v13, vcc_lo, 0
	v_mbcnt_hi_u32_b32 v13, vcc_hi, v13
	v_add_u32_e32 v13, s42, v13
	s_add_i32 s42, s42, s40
	v_cmp_gt_i32_e64 s[0:1], s7, v13
	s_and_b64 s[4:5], vcc, s[0:1]
	s_and_saveexec_b64 s[0:1], s[4:5]
	v_lshl_add_u32 v14, v13, 4, v9
	v_lshl_add_u32 v15, v13, 2, v10
	v_add_u32_e32 v13, 0x2000, v8
	ds_write_b128 v14, v[132:135]
	ds_write_b32 v15, v13
	s_mov_b64 exec, -1
.Lsc_s8:
	s_add_u32 s40, s39, 0x8000
	buffer_load_dwordx4 v[132:135], v6, s[28:31], s40 offen nt
	s_waitcnt vmcnt(9)
	v_or3_b32 v12, v136, v137, v138
	v_bitop3_b32 v12, v12, s9, v139 bitop3:0xc8
	v_cmp_ne_u32_e32 vcc, 0, v12
	s_and_b64 vcc, vcc, s[50:51]
	s_cbranch_vccz .Lsc_s9
	s_bcnt1_i32_b64 s40, vcc
	v_mbcnt_lo_u32_b32 v13, vcc_lo, 0
	v_mbcnt_hi_u32_b32 v13, vcc_hi, v13
	v_add_u32_e32 v13, s42, v13
	s_add_i32 s42, s42, s40
	v_cmp_gt_i32_e64 s[0:1], s7, v13
	s_and_b64 s[4:5], vcc, s[0:1]
	s_and_saveexec_b64 s[0:1], s[4:5]
	v_lshl_add_u32 v14, v13, 4, v9
	v_lshl_add_u32 v15, v13, 2, v10
	v_add_u32_e32 v13, 0x2400, v8
	ds_write_b128 v14, v[136:139]
	ds_write_b32 v15, v13
	s_mov_b64 exec, -1
.Lsc_s9:
	s_add_u32 s40, s39, 0x9000
	buffer_load_dwordx4 v[136:139], v7, s[28:31], s40 offen nt
	s_waitcnt lgkmcnt(0)
	s_add_i32 s42, s42, 1
	v_mov_b32_e32 v12, s42
	ds_write_b32 v11, v12
	s_cmp_eq_u32 s35, s36
	s_cbranch_scc1 .LBB1_384
	s_add_i32 s35, s35, 1
	s_mov_b32 s37, s52
	s_mov_b32 s38, s39
	s_mov_b32 s47, s53
	s_branch .Lsc_row
